# v42 + P11 epilogue: dead zero-initialisations before v_cvt_pk_fp8 (byte-store consumers) removed
# speedup vs baseline: 1.0084x; 1.0003x over previous
.LBB0_1471:
	v_sub_f32_e32 v71, v101, v70
	v_sub_f32_e32 v72, v100, v70
	v_sub_f32_e32 v73, v99, v70
	v_sub_f32_e32 v74, v98, v70
	v_exp_f32_e32 v71, v71
	v_exp_f32_e32 v72, v72
	v_exp_f32_e32 v73, v73
	v_exp_f32_e32 v74, v74
	v_sub_f32_e32 v69, v69, v70
	v_sub_f32_e32 v68, v68, v70
	v_sub_f32_e32 v67, v67, v70
	v_sub_f32_e32 v66, v66, v70
	v_exp_f32_e32 v69, v69
	v_exp_f32_e32 v68, v68
	v_exp_f32_e32 v77, v67
	v_exp_f32_e32 v70, v66
	v_add_f32_e32 v75, v71, v72
	v_add_f32_e32 v76, v73, v74
	v_add_f32_e32 v66, v75, v76
	v_fmac_f32_e32 v66, v185, v0
	v_add_f32_e32 v0, v69, v68
	v_add_f32_e32 v67, v77, v70
	v_add_f32_e32 v0, v0, v67
	v_add_f32_e32 v0, v0, v66
	v_cvt_pk_bf16_f32 v66, v71, v72
	v_cvt_pk_bf16_f32 v68, v69, v68
	v_cvt_pk_bf16_f32 v69, v77, v70
	ds_read_b64_tr_b16 v[70:71],v177
	v_cvt_pk_bf16_f32 v67, v73, v74
	ds_read_b64_tr_b16 v[72:73],v177 offset:8192
	ds_read_b64_tr_b16 v[74:75],v178
	ds_read_b64_tr_b16 v[76:77],v178 offset:8192
	ds_read_b64_tr_b16 v[78:79],v179
	ds_read_b64_tr_b16 v[80:81],v179 offset:8192
	ds_read_b64_tr_b16 v[82:83],v180
	ds_read_b64_tr_b16 v[84:85],v180 offset:8192
	ds_read_b64_tr_b16 v[86:87],v181
	ds_read_b64_tr_b16 v[88:89],v181 offset:8192
	ds_read_b64_tr_b16 v[90:91],v182
	ds_read_b64_tr_b16 v[92:93],v182 offset:8192
	ds_read_b64_tr_b16 v[94:95],v183
	ds_read_b64_tr_b16 v[96:97],v183 offset:8192
	ds_read_b64_tr_b16 v[98:99],v184
	ds_read_b64_tr_b16 v[100:101],v184 offset:8192
	s_waitcnt lgkmcnt(0)
	s_nop 1
	v_mfma_f32_16x16x32_bf16 v[62:65], v[66:69], v[70:73], v[62:65]
	ds_read_b64_tr_b16 v[70:71],v175
	ds_read_b64_tr_b16 v[72:73],v175 offset:8192
	v_mfma_f32_16x16x32_bf16 v[58:61], v[66:69], v[74:77], v[58:61]
	ds_read_b64_tr_b16 v[74:75],v176
	ds_read_b64_tr_b16 v[76:77],v176 offset:8192
	v_mfma_f32_16x16x32_bf16 v[54:57], v[66:69], v[78:81], v[54:57]
	ds_read_b64_tr_b16 v[78:79],v174
	ds_read_b64_tr_b16 v[80:81],v174 offset:8192
	v_mfma_f32_16x16x32_bf16 v[50:53], v[66:69], v[82:85], v[50:53]
	ds_read_b64_tr_b16 v[82:83],v172
	ds_read_b64_tr_b16 v[84:85],v172 offset:8192
	v_mfma_f32_16x16x32_bf16 v[46:49], v[66:69], v[86:89], v[46:49]
	ds_read_b64_tr_b16 v[86:87],v173
	ds_read_b64_tr_b16 v[88:89],v173 offset:8192
	v_mfma_f32_16x16x32_bf16 v[42:45], v[66:69], v[90:93], v[42:45]
	ds_read_b64_tr_b16 v[90:91],v171
	ds_read_b64_tr_b16 v[92:93],v171 offset:8192
	ds_read_b64_tr_b16 v[102:103],v169
	ds_read_b64_tr_b16 v[104:105],v169 offset:8192
	v_mfma_f32_16x16x32_bf16 v[38:41], v[66:69], v[94:97], v[38:41]
	ds_read_b64_tr_b16 v[94:95],v170
	ds_read_b64_tr_b16 v[96:97],v170 offset:8192
	s_waitcnt lgkmcnt(0)
	v_mfma_f32_16x16x32_bf16 v[34:37], v[66:69], v[98:101], v[34:37]
	v_mfma_f32_16x16x32_bf16 v[30:33], v[66:69], v[70:73], v[30:33]
	ds_bpermute_b32 v70, v160, v0
	s_waitcnt lgkmcnt(0)
	s_add_u32 s2, s26, s2
	v_mfma_f32_16x16x32_bf16 v[26:29], v[66:69], v[74:77], v[26:29]
	s_addc_u32 s3, s27, s3
	s_waitcnt lgkmcnt(0)
	v_add_f32_e32 v0, v0, v70
	ds_bpermute_b32 v70, v161, v0
	v_mfma_f32_16x16x32_bf16 v[22:25], v[66:69], v[78:81], v[22:25]
	s_lshl_b32 s17, s15, 1
	s_lshl_b32 s44, s15, 5
	s_mov_b32 s45, -1
	s_waitcnt lgkmcnt(0)
	v_add_f32_e32 v0, v0, v70
	v_div_scale_f32 v70, s[18:19], v0, v0, 1.0
	v_rcp_f32_e32 v71, v70
	v_div_scale_f32 v72, vcc, 1.0, v0, 1.0
	v_mfma_f32_16x16x32_bf16 v[18:21], v[66:69], v[82:85], v[18:21]
	v_fma_f32 v73, -v70, v71, 1.0
	v_fmac_f32_e32 v71, v73, v71
	v_mul_f32_e32 v73, v72, v71
	v_fma_f32 v74, -v70, v73, v72
	v_fmac_f32_e32 v73, v74, v71
	v_fma_f32 v70, -v70, v73, v72
	v_div_fmas_f32 v70, v70, v71, v73
	v_div_fixup_f32 v0, v70, v0, 1.0
	ds_bpermute_b32 v71, v168, v0
	ds_bpermute_b32 v72, v165, v0
	ds_bpermute_b32 v70, v167, v0
	ds_bpermute_b32 v0, v166, v0
	v_mfma_f32_16x16x32_bf16 v[14:17], v[66:69], v[86:89], v[14:17]
	s_waitcnt lgkmcnt(3)
	v_mul_f32_e32 v63, v63, v71
	v_med3_f32 v63, v63, s39, v162
	s_waitcnt lgkmcnt(1)
	v_mul_f32_e32 v58, v58, v70
	v_mfma_f32_16x16x32_bf16 v[10:13], v[66:69], v[90:93], v[10:13]
	v_med3_f32 v58, v58, s39, v162
	v_mul_f32_e32 v54, v54, v70
	v_med3_f32 v54, v54, s39, v162
	v_mfma_f32_16x16x32_bf16 v[6:9], v[66:69], v[102:105], v[6:9]
	v_mul_f32_e32 v50, v50, v70
	v_med3_f32 v50, v50, s39, v162
	v_mul_f32_e32 v46, v46, v70
	v_mfma_f32_16x16x32_bf16 v[2:5], v[66:69], v[94:97], v[2:5]
	v_cvt_pk_fp8_f32 v67, v63, 0
	v_mul_f32_e32 v63, v64, v72
	v_med3_f32 v63, v63, s39, v162
	v_cvt_pk_fp8_f32 v64, v63, 0
	s_waitcnt lgkmcnt(0)
	v_mul_f32_e32 v63, v65, v0
	v_med3_f32 v63, v63, s39, v162
	v_cvt_pk_fp8_f32 v65, v63, 0
	v_cvt_pk_fp8_f32 v63, v58, 0
	v_mul_f32_e32 v58, v59, v71
	v_med3_f32 v58, v58, s39, v162
	v_cvt_pk_fp8_f32 v59, v58, 0
	v_mul_f32_e32 v58, v60, v72
	v_med3_f32 v58, v58, s39, v162
	v_cvt_pk_fp8_f32 v60, v58, 0
	v_mul_f32_e32 v58, v61, v0
	v_med3_f32 v58, v58, s39, v162
	v_cvt_pk_fp8_f32 v61, v58, 0
	v_cvt_pk_fp8_f32 v58, v54, 0
	v_mul_f32_e32 v54, v55, v71
	v_med3_f32 v54, v54, s39, v162
	v_cvt_pk_fp8_f32 v55, v54, 0
	v_mul_f32_e32 v54, v56, v72
	v_med3_f32 v54, v54, s39, v162
	v_cvt_pk_fp8_f32 v56, v54, 0
	v_mul_f32_e32 v54, v57, v0
	v_med3_f32 v54, v54, s39, v162
	v_cvt_pk_fp8_f32 v57, v54, 0
	v_cvt_pk_fp8_f32 v54, v50, 0
	v_mul_f32_e32 v50, v51, v71
	v_med3_f32 v50, v50, s39, v162
	v_cvt_pk_fp8_f32 v51, v50, 0
	v_mul_f32_e32 v50, v52, v72
	v_med3_f32 v50, v50, s39, v162
	v_cvt_pk_fp8_f32 v52, v50, 0
	v_mul_f32_e32 v50, v53, v0
	v_med3_f32 v50, v50, s39, v162
	v_cvt_pk_fp8_f32 v53, v50, 0
	v_med3_f32 v46, v46, s39, v162
	v_cvt_pk_fp8_f32 v50, v46, 0
	v_mul_f32_e32 v46, v47, v71
	v_med3_f32 v46, v46, s39, v162
	v_cvt_pk_fp8_f32 v47, v46, 0
	v_mul_f32_e32 v46, v48, v72
	v_med3_f32 v46, v46, s39, v162
	v_cvt_pk_fp8_f32 v48, v46, 0
	v_mul_f32_e32 v46, v49, v0
	v_med3_f32 v46, v46, s39, v162
	v_mul_f32_e32 v42, v42, v70
	v_cvt_pk_fp8_f32 v49, v46, 0
	v_med3_f32 v42, v42, s39, v162
	v_mov_b32_e32 v46, v1
	v_cvt_pk_fp8_f32 v46, v42, 0
	v_mul_f32_e32 v42, v43, v71
	v_med3_f32 v42, v42, s39, v162
	v_mov_b32_e32 v43, v1
	v_cvt_pk_fp8_f32 v43, v42, 0
	v_mul_f32_e32 v42, v44, v72
	v_med3_f32 v42, v42, s39, v162
	v_mov_b32_e32 v44, v1
	v_cvt_pk_fp8_f32 v44, v42, 0
	v_mul_f32_e32 v42, v45, v0
	v_med3_f32 v42, v42, s39, v162
	v_mov_b32_e32 v45, v1
	v_mul_f32_e32 v38, v38, v70
	v_cvt_pk_fp8_f32 v45, v42, 0
	v_med3_f32 v38, v38, s39, v162
	v_mov_b32_e32 v42, v1
	v_cvt_pk_fp8_f32 v42, v38, 0
	v_mul_f32_e32 v38, v39, v71
	v_med3_f32 v38, v38, s39, v162
	v_mov_b32_e32 v39, v1
	v_cvt_pk_fp8_f32 v39, v38, 0
	v_mul_f32_e32 v38, v40, v72
	v_med3_f32 v38, v38, s39, v162
	v_mov_b32_e32 v40, v1
	v_cvt_pk_fp8_f32 v40, v38, 0
	v_mul_f32_e32 v38, v41, v0
	v_med3_f32 v38, v38, s39, v162
	v_mov_b32_e32 v41, v1
	v_mul_f32_e32 v34, v34, v70
	v_cvt_pk_fp8_f32 v41, v38, 0
	v_med3_f32 v34, v34, s39, v162
	v_mov_b32_e32 v38, v1
	v_cvt_pk_fp8_f32 v38, v34, 0
	v_mul_f32_e32 v34, v35, v71
	v_med3_f32 v34, v34, s39, v162
	v_mov_b32_e32 v35, v1
	v_cvt_pk_fp8_f32 v35, v34, 0
	v_mul_f32_e32 v34, v36, v72
	v_med3_f32 v34, v34, s39, v162
	v_mov_b32_e32 v36, v1
	v_cvt_pk_fp8_f32 v36, v34, 0
	v_mul_f32_e32 v34, v37, v0
	v_med3_f32 v34, v34, s39, v162
	v_mov_b32_e32 v37, v1
	v_mul_f32_e32 v30, v30, v70
	v_cvt_pk_fp8_f32 v37, v34, 0
	v_med3_f32 v30, v30, s39, v162
	v_mov_b32_e32 v34, v1
	v_cvt_pk_fp8_f32 v34, v30, 0
	v_mul_f32_e32 v30, v31, v71
	v_med3_f32 v30, v30, s39, v162
	v_mov_b32_e32 v31, v1
	v_cvt_pk_fp8_f32 v31, v30, 0
	v_mul_f32_e32 v30, v32, v72
	v_med3_f32 v30, v30, s39, v162
	v_mov_b32_e32 v32, v1
	v_cvt_pk_fp8_f32 v32, v30, 0
	v_mul_f32_e32 v30, v33, v0
	v_med3_f32 v30, v30, s39, v162
	v_mov_b32_e32 v33, v1
	v_mul_f32_e32 v26, v26, v70
	v_cvt_pk_fp8_f32 v33, v30, 0
	v_med3_f32 v26, v26, s39, v162
	v_mov_b32_e32 v30, v1
	v_cvt_pk_fp8_f32 v30, v26, 0
	v_mul_f32_e32 v26, v27, v71
	v_med3_f32 v26, v26, s39, v162
	v_mov_b32_e32 v27, v1
	v_cvt_pk_fp8_f32 v27, v26, 0
	v_mul_f32_e32 v26, v28, v72
	v_med3_f32 v26, v26, s39, v162
	v_mov_b32_e32 v28, v1
	v_cvt_pk_fp8_f32 v28, v26, 0
	v_mul_f32_e32 v26, v29, v0
	v_med3_f32 v26, v26, s39, v162
	v_mov_b32_e32 v29, v1
	v_mul_f32_e32 v22, v22, v70
	v_cvt_pk_fp8_f32 v29, v26, 0
	v_med3_f32 v22, v22, s39, v162
	v_mov_b32_e32 v26, v1
	v_cvt_pk_fp8_f32 v26, v22, 0
	v_mul_f32_e32 v22, v23, v71
	v_med3_f32 v22, v22, s39, v162
	v_cvt_pk_fp8_f32 v23, v22, 0
	v_mul_f32_e32 v22, v24, v72
	v_med3_f32 v22, v22, s39, v162
	v_cvt_pk_fp8_f32 v24, v22, 0
	v_mul_f32_e32 v22, v25, v0
	v_med3_f32 v22, v22, s39, v162
	v_mov_b32_e32 v25, v1
	v_mul_f32_e32 v18, v18, v70
	v_cvt_pk_fp8_f32 v25, v22, 0
	v_med3_f32 v18, v18, s39, v162
	v_cvt_pk_fp8_f32 v22, v18, 0
	v_mul_f32_e32 v18, v19, v71
	v_med3_f32 v18, v18, s39, v162
	v_cvt_pk_fp8_f32 v19, v18, 0
	v_mul_f32_e32 v18, v20, v72
	v_med3_f32 v18, v18, s39, v162
	v_cvt_pk_fp8_f32 v20, v18, 0
	v_mul_f32_e32 v18, v21, v0
	v_med3_f32 v18, v18, s39, v162
	v_mul_f32_e32 v14, v14, v70
	v_cvt_pk_fp8_f32 v21, v18, 0
	v_med3_f32 v14, v14, s39, v162
	v_mov_b32_e32 v18, v1
	v_cvt_pk_fp8_f32 v18, v14, 0
	v_mul_f32_e32 v14, v15, v71
	v_med3_f32 v14, v14, s39, v162
	v_cvt_pk_fp8_f32 v15, v14, 0
	v_mul_f32_e32 v14, v16, v72
	v_med3_f32 v14, v14, s39, v162
	v_cvt_pk_fp8_f32 v16, v14, 0
	v_mul_f32_e32 v14, v17, v0
	v_med3_f32 v14, v14, s39, v162
	v_mul_f32_e32 v10, v10, v70
	v_cvt_pk_fp8_f32 v17, v14, 0
	v_med3_f32 v10, v10, s39, v162
	v_mov_b32_e32 v14, v1
	v_cvt_pk_fp8_f32 v14, v10, 0
	v_mul_f32_e32 v10, v11, v71
	v_med3_f32 v10, v10, s39, v162
	v_cvt_pk_fp8_f32 v11, v10, 0
	v_mul_f32_e32 v10, v12, v72
	v_med3_f32 v10, v10, s39, v162
	v_cvt_pk_fp8_f32 v12, v10, 0
	v_mul_f32_e32 v10, v13, v0
	v_med3_f32 v10, v10, s39, v162
	v_mul_f32_e32 v6, v6, v70
	v_cvt_pk_fp8_f32 v13, v10, 0
	v_med3_f32 v6, v6, s39, v162
	v_mov_b32_e32 v10, v1
	v_cvt_pk_fp8_f32 v10, v6, 0
	v_mul_f32_e32 v6, v7, v71
	v_med3_f32 v6, v6, s39, v162
	v_cvt_pk_fp8_f32 v7, v6, 0
	v_mul_f32_e32 v6, v8, v72
	v_med3_f32 v6, v6, s39, v162
	v_mov_b32_e32 v8, v1
	v_cvt_pk_fp8_f32 v8, v6, 0
	v_mul_f32_e32 v6, v9, v0
	v_med3_f32 v6, v6, s39, v162
	v_mul_f32_e32 v2, v2, v70
	v_cvt_pk_fp8_f32 v9, v6, 0
	v_med3_f32 v2, v2, s39, v162
	v_mov_b32_e32 v6, v1
	v_mul_f32_e32 v62, v62, v70
	v_cvt_pk_fp8_f32 v6, v2, 0
	v_mul_f32_e32 v2, v3, v71
	v_med3_f32 v62, v62, s39, v162
	v_med3_f32 v2, v2, s39, v162
	v_cvt_pk_fp8_f32 v66, v62, 0
	v_cvt_pk_fp8_f32 v3, v2, 0
	v_mul_f32_e32 v2, v4, v72
	v_med3_f32 v2, v2, s39, v162
	v_mul_f32_e32 v0, v5, v0
	v_lshlrev_b32_e32 v62, 10, v164
	v_cvt_pk_fp8_f32 v4, v2, 0
	v_med3_f32 v0, v0, s39, v162
	v_mov_b32_e32 v2, v1
	v_add3_u32 v62, s23, v163, v62
	v_cvt_pk_fp8_f32 v2, v0, 0
	ds_write_b8 v62, v66
	ds_write_b8 v62, v67 offset:256
	ds_write_b8 v62, v64 offset:512
	ds_write_b8 v62, v65 offset:768
	ds_write_b8 v62, v63 offset:16
	ds_write_b8 v62, v59 offset:272
	ds_write_b8 v62, v60 offset:528
	ds_write_b8 v62, v61 offset:784
	ds_write_b8 v62, v58 offset:32
	ds_write_b8 v62, v55 offset:288
	ds_write_b8 v62, v56 offset:544
	ds_write_b8 v62, v57 offset:800
	ds_write_b8 v62, v54 offset:48
	ds_write_b8 v62, v51 offset:304
	ds_write_b8 v62, v52 offset:560
	ds_write_b8 v62, v53 offset:816
	ds_write_b8 v62, v50 offset:64
	ds_write_b8 v62, v47 offset:320
	ds_write_b8 v62, v48 offset:576
	ds_write_b8 v62, v49 offset:832
	ds_write_b8 v62, v46 offset:80
	ds_write_b8 v62, v43 offset:336
	ds_write_b8 v62, v44 offset:592
	ds_write_b8 v62, v45 offset:848
	ds_write_b8 v62, v42 offset:96
	ds_write_b8 v62, v39 offset:352
	ds_write_b8 v62, v40 offset:608
	ds_write_b8 v62, v41 offset:864
	ds_write_b8 v62, v38 offset:112
	ds_write_b8 v62, v35 offset:368
	ds_write_b8 v62, v36 offset:624
	ds_write_b8 v62, v37 offset:880
	ds_write_b8 v62, v34 offset:128
	ds_write_b8 v62, v31 offset:384
	ds_write_b8 v62, v32 offset:640
	ds_write_b8 v62, v33 offset:896
	ds_write_b8 v62, v30 offset:144
	ds_write_b8 v62, v27 offset:400
	ds_write_b8 v62, v28 offset:656
	ds_write_b8 v62, v29 offset:912
	ds_write_b8 v62, v26 offset:160
	ds_write_b8 v62, v23 offset:416
	ds_write_b8 v62, v24 offset:672
	ds_write_b8 v62, v25 offset:928
	ds_write_b8 v62, v22 offset:176
	ds_write_b8 v62, v19 offset:432
	ds_write_b8 v62, v20 offset:688
	ds_write_b8 v62, v21 offset:944
	ds_write_b8 v62, v18 offset:192
	ds_write_b8 v62, v15 offset:448
	ds_write_b8 v62, v16 offset:704
	ds_write_b8 v62, v17 offset:960
	ds_write_b8 v62, v14 offset:208
	ds_write_b8 v62, v11 offset:464
	ds_write_b8 v62, v12 offset:720
	ds_write_b8 v62, v13 offset:976
	ds_write_b8 v62, v10 offset:224
	ds_write_b8 v62, v7 offset:480
	ds_write_b8 v62, v8 offset:736
	ds_write_b8 v62, v9 offset:992
	ds_write_b8 v62, v6 offset:240
	ds_write_b8 v62, v3 offset:496
	ds_write_b8 v62, v4 offset:752
	ds_write_b8 v62, v2 offset:1008
	s_waitcnt lgkmcnt(0)
	v_lshl_add_u32 v0, v154, 4, s23
	ds_read_b128 v[2:5], v0
	ds_read_b128 v[6:9], v0 offset:1024
	ds_read_b128 v[10:13], v0 offset:2048
	ds_read_b128 v[14:17], v0 offset:3072
	v_lshl_add_u64 v[18:19], v[154:155], 4, s[2:3]
	s_waitcnt lgkmcnt(3)
	global_store_dwordx4 v[18:19], v[2:5], off nt
	s_waitcnt lgkmcnt(2)
	global_store_dwordx4 v[18:19], v[6:9], off offset:1024 nt
	s_waitcnt lgkmcnt(1)
	global_store_dwordx4 v[18:19], v[10:13], off offset:2048 nt
	s_waitcnt lgkmcnt(0)
	global_store_dwordx4 v[18:19], v[14:17], off offset:3072 nt
	s_waitcnt lgkmcnt(0)
	s_branch .LBB0_1473
